# grid barrier: non-leader workgroups spin on the global generation word directly instead of the per-XCD generation (one wake-up hop fewer), 11 barrier sites
# baseline (speedup 1.0000x reference)
; __device__ __forceinline__ unsigned xb_ld(unsigned* p)              { return __hip_atomic_load(p, __ATOMIC_RELAXED, __HIP_MEMORY_SCOPE_AGENT); }
; __device__ __forceinline__ unsigned xb_add(unsigned* p, unsigned v) { return __hip_atomic_fetch_add(p, v, __ATOMIC_RELAXED, __HIP_MEMORY_SCOPE_AGENT); }
; #define XB_SPIN(cond, bar) do { unsigned _sp = 0; while (cond) { __builtin_amdgcn_s_sleep(1); \
;     if ((++_sp & 255u) == 0u) { if (xb_ld(&(bar)[XB_TMO])) break; if (_sp > XB_SPIN_CAP) { atomicAdd(&(bar)[XB_TMO], 1u); break; } } } } while (0)
; __device__ __forceinline__ void xcd_barrier(const XcdBarrier& b) {
;     ...
;         const unsigned old = xb_add(&bar[XB_XSUB(b.x)], 1u);
;         const unsigned gen = old / nloc;
;         if (old + 1u == (gen + 1u) * nloc) {
;             __builtin_amdgcn_fence(__ATOMIC_RELEASE, "agent");
;             asm volatile("s_waitcnt vmcnt(0)" ::: "memory");
;             const unsigned og = xb_add(&bar[XB_TOP], 1u);
;             const unsigned tg = og / nx;
;             if (og + 1u == (tg + 1u) * nx) xb_add(&bar[XB_TOPGEN], 1u);
;             else XB_SPIN(xb_ld(&bar[XB_TOPGEN]) == tg, bar);
;             __builtin_amdgcn_fence(__ATOMIC_ACQUIRE, "agent");
;             xb_add(&bar[XB_XGEN(b.x)], 1u);
;             asm volatile("s_waitcnt vmcnt(0)" ::: "memory");
;         } else {
;             XB_SPIN(xb_ld(&bar[XB_XGEN(b.x)]) == gen, bar);
.LBB5_404:
	v_readlane_b32 s4, v253, 58
	s_lshl_b32 s4, s4, 8
	s_add_u32 s34, s30, s4
	s_addc_u32 s35, s31, 0
	v_mov_b32_e32 v2, 0x1000
	v_mov_b32_e32 v4, 1
	global_atomic_add v4, v2, v4, s[34:35] offset:1024 sc0
	v_cvt_f32_u32_e32 v2, v3
	v_sub_u32_e32 v5, 0, v3
	v_rcp_iflag_f32_e32 v2, v2
	s_nop 0
	v_mul_f32_e32 v2, 0x4f7ffffe, v2
	v_cvt_u32_f32_e32 v2, v2
	v_mul_lo_u32 v5, v5, v2
	v_mul_hi_u32 v5, v2, v5
	v_add_u32_e32 v2, v2, v5
	s_waitcnt vmcnt(0)
	v_mul_hi_u32 v2, v4, v2
	v_mul_lo_u32 v5, v2, v3
	v_sub_u32_e32 v5, v4, v5
	v_add_u32_e32 v6, 1, v2
	v_cmp_ge_u32_e32 vcc, v5, v3
	v_add_u32_e32 v4, 1, v4
	s_nop 0
	v_cndmask_b32_e32 v2, v2, v6, vcc
	v_sub_u32_e32 v6, v5, v3
	v_cndmask_b32_e32 v5, v5, v6, vcc
	v_add_u32_e32 v6, 1, v2
	v_cmp_ge_u32_e32 vcc, v5, v3
	s_nop 1
	v_cndmask_b32_e32 v2, v2, v6, vcc
	v_mul_lo_u32 v5, v3, v2
	v_add_u32_e32 v3, v5, v3
	v_cmp_ne_u32_e32 vcc, v4, v3
	s_and_saveexec_b64 s[4:5], vcc
	s_xor_b64 s[36:37], exec, s[4:5]
	s_cbranch_execz .LBB5_418
	s_waitcnt lgkmcnt(0)
	v_mov_b32_e32 v1, 0x3100
	global_load_dword v1, v1, s[30:31] offset:1024 sc1
	s_add_u32 s68, s30, 0x3500
	s_addc_u32 s69, s31, 0
	s_waitcnt vmcnt(0)
	v_cmp_eq_u32_e32 vcc, v1, v2
	s_and_saveexec_b64 s[38:39], vcc
	s_cbranch_execz .LBB5_417
	s_mov_b32 s4, 1
	s_mov_b64 s[70:71], 0
	v_mov_b32_e32 v1, 0
	s_branch .LBB5_408

; __device__ __forceinline__ unsigned xb_ld(unsigned* p)              { return __hip_atomic_load(p, __ATOMIC_RELAXED, __HIP_MEMORY_SCOPE_AGENT); }
; __device__ __forceinline__ unsigned xb_add(unsigned* p, unsigned v) { return __hip_atomic_fetch_add(p, v, __ATOMIC_RELAXED, __HIP_MEMORY_SCOPE_AGENT); }
; #define XB_SPIN(cond, bar) do { unsigned _sp = 0; while (cond) { __builtin_amdgcn_s_sleep(1); \
;     if ((++_sp & 255u) == 0u) { if (xb_ld(&(bar)[XB_TMO])) break; if (_sp > XB_SPIN_CAP) { atomicAdd(&(bar)[XB_TMO], 1u); break; } } } } while (0)
; __device__ __forceinline__ void xcd_barrier(const XcdBarrier& b) {
;     ...
;         const unsigned old = xb_add(&bar[XB_XSUB(b.x)], 1u);
;         const unsigned gen = old / nloc;
;         if (old + 1u == (gen + 1u) * nloc) {
;             __builtin_amdgcn_fence(__ATOMIC_RELEASE, "agent");
;             asm volatile("s_waitcnt vmcnt(0)" ::: "memory");
;             const unsigned og = xb_add(&bar[XB_TOP], 1u);
;             const unsigned tg = og / nx;
;             if (og + 1u == (tg + 1u) * nx) xb_add(&bar[XB_TOPGEN], 1u);
;             else XB_SPIN(xb_ld(&bar[XB_TOPGEN]) == tg, bar);
;             __builtin_amdgcn_fence(__ATOMIC_ACQUIRE, "agent");
;             xb_add(&bar[XB_XGEN(b.x)], 1u);
;             asm volatile("s_waitcnt vmcnt(0)" ::: "memory");
;         } else {
;             XB_SPIN(xb_ld(&bar[XB_XGEN(b.x)]) == gen, bar);
.LBB5_836:
	v_readlane_b32 s3, v253, 58
	s_lshl_b32 s3, s3, 8
	s_add_u32 s6, s30, s3
	s_addc_u32 s7, s31, 0
	v_mov_b32_e32 v2, 0x1000
	v_mov_b32_e32 v4, 1
	global_atomic_add v4, v2, v4, s[6:7] offset:1024 sc0
	v_cvt_f32_u32_e32 v2, v3
	v_sub_u32_e32 v5, 0, v3
	v_rcp_iflag_f32_e32 v2, v2
	s_nop 0
	v_mul_f32_e32 v2, 0x4f7ffffe, v2
	v_cvt_u32_f32_e32 v2, v2
	v_mul_lo_u32 v5, v5, v2
	v_mul_hi_u32 v5, v2, v5
	v_add_u32_e32 v2, v2, v5
	s_waitcnt vmcnt(0)
	v_mul_hi_u32 v2, v4, v2
	v_mul_lo_u32 v5, v2, v3
	v_sub_u32_e32 v5, v4, v5
	v_add_u32_e32 v6, 1, v2
	v_cmp_ge_u32_e32 vcc, v5, v3
	v_add_u32_e32 v4, 1, v4
	s_nop 0
	v_cndmask_b32_e32 v2, v2, v6, vcc
	v_sub_u32_e32 v6, v5, v3
	v_cndmask_b32_e32 v5, v5, v6, vcc
	v_add_u32_e32 v6, 1, v2
	v_cmp_ge_u32_e32 vcc, v5, v3
	s_nop 1
	v_cndmask_b32_e32 v2, v2, v6, vcc
	v_mul_lo_u32 v5, v3, v2
	v_add_u32_e32 v3, v5, v3
	v_cmp_ne_u32_e32 vcc, v4, v3
	s_and_saveexec_b64 s[8:9], vcc
	s_xor_b64 s[8:9], exec, s[8:9]
	s_cbranch_execz .LBB5_850
	s_waitcnt lgkmcnt(0)
	v_mov_b32_e32 v1, 0x3100
	global_load_dword v1, v1, s[30:31] offset:1024 sc1
	s_add_u32 s12, s30, 0x3500
	s_addc_u32 s13, s31, 0
	s_waitcnt vmcnt(0)
	v_cmp_eq_u32_e32 vcc, v1, v2
	s_and_saveexec_b64 s[10:11], vcc
	s_cbranch_execz .LBB5_849
	s_mov_b32 s3, 1
	s_mov_b64 s[14:15], 0
	v_mov_b32_e32 v1, 0
	s_branch .LBB5_840

; __device__ __forceinline__ unsigned xb_ld(unsigned* p)              { return __hip_atomic_load(p, __ATOMIC_RELAXED, __HIP_MEMORY_SCOPE_AGENT); }
; __device__ __forceinline__ unsigned xb_add(unsigned* p, unsigned v) { return __hip_atomic_fetch_add(p, v, __ATOMIC_RELAXED, __HIP_MEMORY_SCOPE_AGENT); }
; #define XB_SPIN(cond, bar) do { unsigned _sp = 0; while (cond) { __builtin_amdgcn_s_sleep(1); \
;     if ((++_sp & 255u) == 0u) { if (xb_ld(&(bar)[XB_TMO])) break; if (_sp > XB_SPIN_CAP) { atomicAdd(&(bar)[XB_TMO], 1u); break; } } } } while (0)
; __device__ __forceinline__ void xcd_barrier(const XcdBarrier& b) {
;     ...
;         const unsigned old = xb_add(&bar[XB_XSUB(b.x)], 1u);
;         const unsigned gen = old / nloc;
;         if (old + 1u == (gen + 1u) * nloc) {
;             __builtin_amdgcn_fence(__ATOMIC_RELEASE, "agent");
;             asm volatile("s_waitcnt vmcnt(0)" ::: "memory");
;             const unsigned og = xb_add(&bar[XB_TOP], 1u);
;             const unsigned tg = og / nx;
;             if (og + 1u == (tg + 1u) * nx) xb_add(&bar[XB_TOPGEN], 1u);
;             else XB_SPIN(xb_ld(&bar[XB_TOPGEN]) == tg, bar);
;             __builtin_amdgcn_fence(__ATOMIC_ACQUIRE, "agent");
;             xb_add(&bar[XB_XGEN(b.x)], 1u);
;             asm volatile("s_waitcnt vmcnt(0)" ::: "memory");
;         } else {
;             XB_SPIN(xb_ld(&bar[XB_XGEN(b.x)]) == gen, bar);
.LBB5_1285:
	v_readlane_b32 s3, v253, 58
	s_lshl_b32 s3, s3, 8
	s_add_u32 s4, s30, s3
	s_addc_u32 s5, s31, 0
	v_mov_b32_e32 v2, 0x1000
	v_mov_b32_e32 v4, 1
	global_atomic_add v4, v2, v4, s[4:5] offset:1024 sc0
	v_cvt_f32_u32_e32 v2, v3
	v_sub_u32_e32 v5, 0, v3
	v_rcp_iflag_f32_e32 v2, v2
	s_nop 0
	v_mul_f32_e32 v2, 0x4f7ffffe, v2
	v_cvt_u32_f32_e32 v2, v2
	v_mul_lo_u32 v5, v5, v2
	v_mul_hi_u32 v5, v2, v5
	v_add_u32_e32 v2, v2, v5
	s_waitcnt vmcnt(0)
	v_mul_hi_u32 v2, v4, v2
	v_mul_lo_u32 v5, v2, v3
	v_sub_u32_e32 v5, v4, v5
	v_add_u32_e32 v6, 1, v2
	v_cmp_ge_u32_e32 vcc, v5, v3
	v_add_u32_e32 v4, 1, v4
	s_nop 0
	v_cndmask_b32_e32 v2, v2, v6, vcc
	v_sub_u32_e32 v6, v5, v3
	v_cndmask_b32_e32 v5, v5, v6, vcc
	v_add_u32_e32 v6, 1, v2
	v_cmp_ge_u32_e32 vcc, v5, v3
	s_nop 1
	v_cndmask_b32_e32 v2, v2, v6, vcc
	v_mul_lo_u32 v5, v3, v2
	v_add_u32_e32 v3, v5, v3
	v_cmp_ne_u32_e32 vcc, v4, v3
	s_and_saveexec_b64 s[8:9], vcc
	s_xor_b64 s[8:9], exec, s[8:9]
	s_cbranch_execz .LBB5_1299
	s_waitcnt lgkmcnt(0)
	v_mov_b32_e32 v1, 0x3100
	global_load_dword v1, v1, s[30:31] offset:1024 sc1
	s_add_u32 s12, s30, 0x3500
	s_addc_u32 s13, s31, 0
	s_waitcnt vmcnt(0)
	v_cmp_eq_u32_e32 vcc, v1, v2
	s_and_saveexec_b64 s[10:11], vcc
	s_cbranch_execz .LBB5_1298
	s_mov_b32 s3, 1
	s_mov_b64 s[14:15], 0
	v_mov_b32_e32 v1, 0
	s_branch .LBB5_1289

; __device__ __forceinline__ unsigned xb_ld(unsigned* p)              { return __hip_atomic_load(p, __ATOMIC_RELAXED, __HIP_MEMORY_SCOPE_AGENT); }
; __device__ __forceinline__ unsigned xb_add(unsigned* p, unsigned v) { return __hip_atomic_fetch_add(p, v, __ATOMIC_RELAXED, __HIP_MEMORY_SCOPE_AGENT); }
; #define XB_SPIN(cond, bar) do { unsigned _sp = 0; while (cond) { __builtin_amdgcn_s_sleep(1); \
;     if ((++_sp & 255u) == 0u) { if (xb_ld(&(bar)[XB_TMO])) break; if (_sp > XB_SPIN_CAP) { atomicAdd(&(bar)[XB_TMO], 1u); break; } } } } while (0)
; __device__ __forceinline__ void xcd_barrier(const XcdBarrier& b) {
;     ...
;         const unsigned old = xb_add(&bar[XB_XSUB(b.x)], 1u);
;         const unsigned gen = old / nloc;
;         if (old + 1u == (gen + 1u) * nloc) {
;             __builtin_amdgcn_fence(__ATOMIC_RELEASE, "agent");
;             asm volatile("s_waitcnt vmcnt(0)" ::: "memory");
;             const unsigned og = xb_add(&bar[XB_TOP], 1u);
;             const unsigned tg = og / nx;
;             if (og + 1u == (tg + 1u) * nx) xb_add(&bar[XB_TOPGEN], 1u);
;             else XB_SPIN(xb_ld(&bar[XB_TOPGEN]) == tg, bar);
;             __builtin_amdgcn_fence(__ATOMIC_ACQUIRE, "agent");
;             xb_add(&bar[XB_XGEN(b.x)], 1u);
;             asm volatile("s_waitcnt vmcnt(0)" ::: "memory");
;         } else {
;             XB_SPIN(xb_ld(&bar[XB_XGEN(b.x)]) == gen, bar);
.LBB5_1631:
	v_readlane_b32 s4, v253, 58
	s_lshl_b32 s4, s4, 8
	s_add_u32 s4, s30, s4
	s_addc_u32 s5, s31, 0
	v_mov_b32_e32 v2, 0x1000
	v_mov_b32_e32 v4, 1
	global_atomic_add v4, v2, v4, s[4:5] offset:1024 sc0
	v_cvt_f32_u32_e32 v2, v3
	v_sub_u32_e32 v5, 0, v3
	v_rcp_iflag_f32_e32 v2, v2
	s_nop 0
	v_mul_f32_e32 v2, 0x4f7ffffe, v2
	v_cvt_u32_f32_e32 v2, v2
	v_mul_lo_u32 v5, v5, v2
	v_mul_hi_u32 v5, v2, v5
	v_add_u32_e32 v2, v2, v5
	s_waitcnt vmcnt(0)
	v_mul_hi_u32 v2, v4, v2
	v_mul_lo_u32 v5, v2, v3
	v_sub_u32_e32 v5, v4, v5
	v_add_u32_e32 v6, 1, v2
	v_cmp_ge_u32_e32 vcc, v5, v3
	v_add_u32_e32 v4, 1, v4
	s_nop 0
	v_cndmask_b32_e32 v2, v2, v6, vcc
	v_sub_u32_e32 v6, v5, v3
	v_cndmask_b32_e32 v5, v5, v6, vcc
	v_add_u32_e32 v6, 1, v2
	v_cmp_ge_u32_e32 vcc, v5, v3
	s_nop 1
	v_cndmask_b32_e32 v2, v2, v6, vcc
	v_mul_lo_u32 v5, v3, v2
	v_add_u32_e32 v3, v5, v3
	v_cmp_ne_u32_e32 vcc, v4, v3
	s_and_saveexec_b64 s[6:7], vcc
	s_xor_b64 s[6:7], exec, s[6:7]
	s_cbranch_execz .LBB5_1645
	s_waitcnt lgkmcnt(0)
	v_mov_b32_e32 v1, 0x3100
	global_load_dword v1, v1, s[30:31] offset:1024 sc1
	s_add_u32 s10, s30, 0x3500
	s_addc_u32 s11, s31, 0
	s_waitcnt vmcnt(0)
	v_cmp_eq_u32_e32 vcc, v1, v2
	s_and_saveexec_b64 s[8:9], vcc
	s_cbranch_execz .LBB5_1644
	s_mov_b32 s27, 1
	s_mov_b64 s[12:13], 0
	v_mov_b32_e32 v1, 0
	s_branch .LBB5_1635

; __device__ __forceinline__ unsigned xb_ld(unsigned* p)              { return __hip_atomic_load(p, __ATOMIC_RELAXED, __HIP_MEMORY_SCOPE_AGENT); }
; __device__ __forceinline__ unsigned xb_add(unsigned* p, unsigned v) { return __hip_atomic_fetch_add(p, v, __ATOMIC_RELAXED, __HIP_MEMORY_SCOPE_AGENT); }
; #define XB_SPIN(cond, bar) do { unsigned _sp = 0; while (cond) { __builtin_amdgcn_s_sleep(1); \
;     if ((++_sp & 255u) == 0u) { if (xb_ld(&(bar)[XB_TMO])) break; if (_sp > XB_SPIN_CAP) { atomicAdd(&(bar)[XB_TMO], 1u); break; } } } } while (0)
; __device__ __forceinline__ void xcd_barrier(const XcdBarrier& b) {
;     ...
;         const unsigned old = xb_add(&bar[XB_XSUB(b.x)], 1u);
;         const unsigned gen = old / nloc;
;         if (old + 1u == (gen + 1u) * nloc) {
;             __builtin_amdgcn_fence(__ATOMIC_RELEASE, "agent");
;             asm volatile("s_waitcnt vmcnt(0)" ::: "memory");
;             const unsigned og = xb_add(&bar[XB_TOP], 1u);
;             const unsigned tg = og / nx;
;             if (og + 1u == (tg + 1u) * nx) xb_add(&bar[XB_TOPGEN], 1u);
;             else XB_SPIN(xb_ld(&bar[XB_TOPGEN]) == tg, bar);
;             __builtin_amdgcn_fence(__ATOMIC_ACQUIRE, "agent");
;             xb_add(&bar[XB_XGEN(b.x)], 1u);
;             asm volatile("s_waitcnt vmcnt(0)" ::: "memory");
;         } else {
;             XB_SPIN(xb_ld(&bar[XB_XGEN(b.x)]) == gen, bar);
.LBB5_1704:
	v_readlane_b32 s4, v253, 58
	s_lshl_b32 s4, s4, 8
	s_add_u32 s4, s30, s4
	s_addc_u32 s5, s31, 0
	v_mov_b32_e32 v2, 0x1000
	v_mov_b32_e32 v4, 1
	global_atomic_add v4, v2, v4, s[4:5] offset:1024 sc0
	v_cvt_f32_u32_e32 v2, v3
	v_sub_u32_e32 v5, 0, v3
	v_rcp_iflag_f32_e32 v2, v2
	s_nop 0
	v_mul_f32_e32 v2, 0x4f7ffffe, v2
	v_cvt_u32_f32_e32 v2, v2
	v_mul_lo_u32 v5, v5, v2
	v_mul_hi_u32 v5, v2, v5
	v_add_u32_e32 v2, v2, v5
	s_waitcnt vmcnt(0)
	v_mul_hi_u32 v2, v4, v2
	v_mul_lo_u32 v5, v2, v3
	v_sub_u32_e32 v5, v4, v5
	v_add_u32_e32 v6, 1, v2
	v_cmp_ge_u32_e32 vcc, v5, v3
	v_add_u32_e32 v4, 1, v4
	s_nop 0
	v_cndmask_b32_e32 v2, v2, v6, vcc
	v_sub_u32_e32 v6, v5, v3
	v_cndmask_b32_e32 v5, v5, v6, vcc
	v_add_u32_e32 v6, 1, v2
	v_cmp_ge_u32_e32 vcc, v5, v3
	s_nop 1
	v_cndmask_b32_e32 v2, v2, v6, vcc
	v_mul_lo_u32 v5, v3, v2
	v_add_u32_e32 v3, v5, v3
	v_cmp_ne_u32_e32 vcc, v4, v3
	s_and_saveexec_b64 s[6:7], vcc
	s_xor_b64 s[6:7], exec, s[6:7]
	s_cbranch_execz .LBB5_1718
	s_waitcnt lgkmcnt(0)
	v_mov_b32_e32 v1, 0x3100
	global_load_dword v1, v1, s[30:31] offset:1024 sc1
	s_add_u32 s10, s30, 0x3500
	s_addc_u32 s11, s31, 0
	s_waitcnt vmcnt(0)
	v_cmp_eq_u32_e32 vcc, v1, v2
	s_and_saveexec_b64 s[8:9], vcc
	s_cbranch_execz .LBB5_1717
	s_mov_b32 s25, 1
	s_mov_b64 s[12:13], 0
	v_mov_b32_e32 v1, 0
	s_branch .LBB5_1708
